# W11 + plain/silu in-proj epilogue no longer drains the next unit's in-flight LDS-DMA prefetch (the wait only guards the rotary table loads)
# speedup vs baseline: 1.0067x; 1.0018x over previous
.LBB0_314:
	s_mov_b32 s0, -1
	v_mov_b32_e32 v195, 4
	v_mbcnt_lo_u32_b32 v40, s0, 0
	v_mbcnt_hi_u32_b32 v41, s0, v40
	s_lshl_b32 s0, s22, 8
	v_lshrrev_b32_e32 v40, 4, v41
	s_or_b32 s0, s0, s85
	v_lshl_add_u32 v193, v40, 3, s0
	s_movk_i32 s0, 0xc00
	v_mul_hi_i32 v42, v193, s6
	v_cmp_gt_i32_e64 s[42:43], s0, v193
	v_add_u32_e32 v203, 0xfffff400, v193
	v_mov_b32_e32 v196, 0x3000000
	v_lshrrev_b32_e32 v201, 31, v42
	v_lshrrev_b32_e32 v204, 7, v42
	v_mov_b32_e32 v200, 0x3000000
	v_mov_b32_e32 v202, 4
	s_and_saveexec_b64 s[0:1], s[42:43]
	v_add_u32_e32 v42, v204, v201
	s_mov_b32 s4, 0xc00000
	v_mul_lo_u32 v200, v42, s4
	v_mov_b32_e32 v202, 6
	v_mov_b32_e32 v203, v193
	s_or_b64 exec, exec, s[0:1]
	v_add_u32_e32 v194, 0x80, v193
	s_movk_i32 s0, 0xb80
	v_mul_hi_i32 v42, v194, s6
	v_cmp_gt_i32_e64 s[44:45], s0, v193
	v_add_u32_e32 v199, 0xfffff480, v193
	v_lshrrev_b32_e32 v197, 31, v42
	v_lshrrev_b32_e32 v198, 7, v42
	s_and_saveexec_b64 s[0:1], s[44:45]
	v_add_u32_e32 v42, v198, v197
	s_mov_b32 s4, 0xc00000
	v_mul_lo_u32 v196, v42, s4
	v_mov_b32_e32 v195, 6
	v_mov_b32_e32 v199, v194
	s_or_b64 exec, exec, s[0:1]
	s_lshl_b32 s8, s2, 8
	s_add_i32 s8, s8, s84
	s_cmp_lt_i32 s22, 6
	s_cselect_b64 s[80:81], -1, 0
	s_add_i32 s0, s22, -9
	s_sub_i32 s1, s22, 20
	s_min_u32 s0, s0, s1
	s_cmp_lt_u32 s0, 3
	v_and_b32_e32 v192, 15, v41
	s_cselect_b64 s[0:1], -1, 0
	s_and_b64 vcc, exec, s[80:81]
	s_cbranch_vccnz .Lepiz_m1
	s_and_b64 vcc, exec, s[0:1]
	s_cbranch_vccnz .Lepiz_m2
	v_cndmask_b32_e64 v172, 0, 1, s[80:81]
	v_cmp_ne_u32_e64 s[40:41], 1, v172
	s_mov_b64 s[4:5], -1
	v_cndmask_b32_e64 v159, 0, 1, s[0:1]
	v_cmp_ne_u32_e64 s[38:39], 1, v159
	v_mov_b32_e32 v156, v148
	v_mov_b32_e32 v179, v149
	v_mov_b32_e32 v180, v150
	v_mov_b32_e32 v182, v151
	v_mov_b32_e32 v178, v144
	v_mov_b32_e32 v185, v145
	v_mov_b32_e32 v186, v146
	v_mov_b32_e32 v188, v147
	s_lshr_b32 s0, s8, 4
	s_and_b32 s4, s0, 0xfc
	s_ashr_i32 s0, s2, 31
	s_lshr_b32 s0, s0, 28
	s_add_i32 s0, s2, s0
	s_ashr_i32 s13, s0, 4
	v_add_u32_e32 v144, v204, v201
	s_movk_i32 s0, 0x300
	v_mul_lo_u32 v144, v144, s0
	v_sub_u32_e32 v144, v193, v144
	v_cndmask_b32_e64 v146, v203, v144, s[42:43]
	v_lshrrev_b32_e32 v144, 7, v146
	v_mad_u64_u32 v[144:145], s[0:1], v202, s13, v[144:145]
	v_lshlrev_b32_e32 v145, 4, v146
	v_lshl_add_u32 v144, v144, 19, v200
	v_and_b32_e32 v145, 0x600, v145
	v_and_b32_e32 v146, 31, v146
	v_or3_b32 v146, v144, v145, v146
	v_add_u32_e32 v144, 0xfffff200, v193
	v_mul_hi_i32 v145, v144, s6
	v_lshrrev_b32_e32 v147, 31, v145
	v_ashrrev_i32_e32 v145, 6, v145
	v_add_u32_e32 v145, v145, v147
	v_mul_i32_i24_e32 v147, 0x180, v145
	v_sub_u32_e32 v144, v144, v147
	v_mul_i32_i24_e32 v147, 0x2aab, v144
	v_mov_b32_e32 v148, 4
	v_ashrrev_i16_sdwa v148, v148, v147 dst_sel:DWORD dst_unused:UNUSED_PAD src0_sel:DWORD src1_sel:WORD_1
	v_lshrrev_b32_e32 v147, 31, v147
	v_add_u16_e32 v147, v148, v147
	v_mul_lo_u16_e32 v148, 0x60, v147
	v_sub_u16_e32 v144, v144, v148
	s_lshl_b32 s5, s13, 2
	v_bfe_i32 v148, v144, 0, 16
	v_mul_i32_i24_e32 v144, 0x600000, v145
	v_and_or_b32 v144, v148, 31, v144
	v_add_u32_e32 v145, s5, v147
	s_mov_b32 s0, 0x60000
	v_lshlrev_b32_e32 v147, 4, v148
	v_mad_u64_u32 v[144:145], s[0:1], v145, s0, v[144:145]
	v_and_b32_e32 v147, 0xfffffe00, v147
	s_mov_b32 s0, 0x3800000
	v_add3_u32 v147, v144, v147, s0
	v_add_u32_e32 v144, 0xffffef00, v193
	v_mul_hi_i32 v145, v144, s6
	v_lshrrev_b32_e32 v148, 31, v145
	v_ashrrev_i32_e32 v145, 7, v145
	v_add_u32_e32 v145, v145, v148
	v_mul_i32_i24_e32 v148, 0x300, v145
	v_sub_u32_e32 v144, v144, v148
	v_mul_i32_i24_e32 v148, 0x2aab, v144
	v_mov_b32_e32 v149, 5
	v_ashrrev_i16_sdwa v149, v149, v148 dst_sel:DWORD dst_unused:UNUSED_PAD src0_sel:DWORD src1_sel:WORD_1
	v_lshrrev_b32_e32 v148, 31, v148
	v_add_u16_e32 v148, v149, v148
	v_mul_lo_u16_e32 v149, 0xc0, v148
	v_sub_u16_e32 v144, v144, v149
	s_mov_b32 s0, 0xc00000
	v_bfe_i32 v149, v144, 0, 16
	v_mul_lo_u32 v144, v145, s0
	v_and_or_b32 v144, v149, 31, v144
	v_add_u32_e32 v145, s5, v148
	s_mov_b32 s0, 0xc0000
	v_lshlrev_b32_e32 v148, 4, v149
	v_mad_u64_u32 v[144:145], s[0:1], v145, s0, v[144:145]
	v_and_b32_e32 v148, 0xfffffe00, v148
	s_mov_b32 s0, 0x4400000
	v_add3_u32 v144, v144, v148, s0
	s_movk_i32 s0, 0xe00
	s_lshl_b32 s2, s13, 16
	v_cmp_gt_i32_e32 vcc, s0, v193
	s_movk_i32 s0, 0x1710
	s_add_i32 s2, s2, 0x5bfe900
	v_cmp_gt_u32_e64 s[42:43], s0, v193
	s_movk_i32 s0, 0x1700
	v_add_u32_e32 v145, s2, v193
	v_cndmask_b32_e64 v149, 0, v237, s[42:43]
	v_cmp_gt_i32_e64 s[46:47], s0, v193
	s_movk_i32 s0, 0x1100
	v_cndmask_b32_e32 v148, v236, v218, vcc
	v_cndmask_b32_e64 v149, v149, v239, s[46:47]
	v_cmp_gt_i32_e64 s[42:43], s0, v193
	v_cndmask_b32_e64 v144, v145, v144, s[46:47]
	s_nop 0
	v_cndmask_b32_e64 v159, v149, v148, s[42:43]
	v_cndmask_b32_e64 v144, v144, v147, s[42:43]
	v_cndmask_b32_e32 v181, v144, v146, vcc
	v_cvt_pk_bf16_f32 v144, v156, v179
	v_cvt_pk_bf16_f32 v145, v180, v182
	v_cmp_ne_u32_e64 s[42:43], 0, v159
	v_cndmask_b32_e64 v180, 4, 5, s[46:47]
	v_cvt_pk_bf16_f32 v146, v178, v185
	v_cvt_pk_bf16_f32 v147, v186, v188
	s_and_saveexec_b64 s[0:1], s[42:43]
	v_mul_u32_u24_e32 v148, s4, v159
	v_lshl_or_b32 v148, v192, v180, v148
	v_add_u32_e32 v212, v148, v181
	v_lshl_add_u64 v[148:149], v[212:213], 1, s[52:53]
	global_store_dwordx4 v[148:149], v[144:147], off nt
	s_nop 1
	s_or_b64 exec, exec, s[0:1]
	s_mov_b64 s[0:1], -1
	v_mov_b32_e32 v144, v136
	v_mov_b32_e32 v145, v137
	v_mov_b32_e32 v146, v138
	v_mov_b32_e32 v148, v139
	v_mov_b32_e32 v147, v132
	v_mov_b32_e32 v151, v133
	v_mov_b32_e32 v178, v134
	v_mov_b32_e32 v156, v135
	v_add_u32_e32 v132, v198, v197
	s_movk_i32 s0, 0x300
	v_mul_lo_u32 v132, v132, s0
	v_sub_u32_e32 v132, v194, v132
	v_cndmask_b32_e64 v134, v199, v132, s[44:45]
	v_lshrrev_b32_e32 v132, 7, v134
	v_mad_u64_u32 v[132:133], s[0:1], v195, s13, v[132:133]
	v_lshlrev_b32_e32 v133, 4, v134
	v_lshl_add_u32 v132, v132, 19, v196
	v_and_b32_e32 v133, 0x600, v133
	v_and_b32_e32 v134, 31, v134
	v_or3_b32 v134, v132, v133, v134
	v_add_u32_e32 v132, 0xfffff280, v193
	v_mul_hi_i32 v133, v132, s6
	v_lshrrev_b32_e32 v135, 31, v133
	v_ashrrev_i32_e32 v133, 6, v133
	v_add_u32_e32 v133, v133, v135
	v_mul_i32_i24_e32 v135, 0x180, v133
	v_sub_u32_e32 v132, v132, v135
	v_mul_i32_i24_e32 v135, 0x2aab, v132
	v_lshrrev_b32_e32 v136, 31, v135
	v_ashrrev_i32_e32 v135, 20, v135
	v_add_u16_e32 v135, v135, v136
	v_mul_lo_u16_e32 v136, 0x60, v135
	v_sub_u16_e32 v132, v132, v136
	v_bfe_i32 v136, v132, 0, 16
	v_mul_i32_i24_e32 v132, 0x600000, v133
	v_and_or_b32 v132, v136, 31, v132
	v_add_u32_e32 v133, s5, v135
	s_mov_b32 s0, 0x60000
	v_lshlrev_b32_e32 v135, 4, v136
	v_mad_u64_u32 v[132:133], s[0:1], v133, s0, v[132:133]
	v_and_b32_e32 v135, 0xfffffe00, v135
	s_mov_b32 s0, 0x3800000
	v_add3_u32 v135, v132, v135, s0
	v_add_u32_e32 v132, 0xffffef80, v193
	v_mul_hi_i32 v133, v132, s6
	v_lshrrev_b32_e32 v136, 31, v133
	v_ashrrev_i32_e32 v133, 7, v133
	v_add_u32_e32 v133, v133, v136
	v_mul_i32_i24_e32 v136, 0x300, v133
	v_sub_u32_e32 v132, v132, v136
	v_mul_i32_i24_e32 v136, 0x2aab, v132
	v_lshrrev_b32_e32 v137, 31, v136
	v_ashrrev_i32_e32 v136, 21, v136
	v_add_u16_e32 v136, v136, v137
	v_mul_lo_u16_e32 v137, 0xc0, v136
	v_sub_u16_e32 v132, v132, v137
	s_mov_b32 s0, 0xc00000
	v_bfe_i32 v137, v132, 0, 16
	v_mul_lo_u32 v132, v133, s0
	v_and_or_b32 v132, v137, 31, v132
	v_add_u32_e32 v133, s5, v136
	s_mov_b32 s0, 0xc0000
	v_lshlrev_b32_e32 v136, 4, v137
	v_mad_u64_u32 v[132:133], s[0:1], v133, s0, v[132:133]
	v_and_b32_e32 v136, 0xfffffe00, v136
	s_mov_b32 s0, 0x4400000
	v_add3_u32 v132, v132, v136, s0
	s_movk_i32 s0, 0xd80
	v_cmp_gt_i32_e32 vcc, s0, v193
	s_movk_i32 s0, 0x1710
	v_cmp_gt_u32_e64 s[44:45], s0, v194
	s_movk_i32 s0, 0x1680
	v_add_u32_e32 v133, s2, v194
	v_cndmask_b32_e64 v137, 0, v237, s[44:45]
	v_cmp_gt_i32_e64 s[46:47], s0, v193
	s_movk_i32 s0, 0x1080
	v_cndmask_b32_e32 v136, v236, v218, vcc
	v_cndmask_b32_e64 v137, v137, v239, s[46:47]
	v_cmp_gt_i32_e64 s[44:45], s0, v193
	v_cndmask_b32_e64 v132, v133, v132, s[46:47]
	s_nop 0
	v_cndmask_b32_e64 v158, v137, v136, s[44:45]
	v_cndmask_b32_e64 v132, v132, v135, s[44:45]
	v_cndmask_b32_e32 v172, v132, v134, vcc
	v_cvt_pk_bf16_f32 v132, v144, v145
	v_cmp_ne_u32_e64 s[44:45], 0, v158
	v_cndmask_b32_e64 v145, 4, 5, s[46:47]
	v_cvt_pk_bf16_f32 v133, v146, v148
	v_cvt_pk_bf16_f32 v134, v147, v151
	v_cvt_pk_bf16_f32 v135, v178, v156
	s_and_saveexec_b64 s[0:1], s[44:45]
	v_mul_u32_u24_e32 v136, s4, v158
	v_lshl_or_b32 v136, v192, v145, v136
	v_add_u32_e32 v212, v136, v172
	v_lshl_add_u64 v[136:137], v[212:213], 1, s[52:53]
	global_store_dwordx4 v[136:137], v[132:135], off nt
	s_nop 1
	s_or_b64 exec, exec, s[0:1]
	s_or_b32 s2, s4, 1
	v_cvt_pk_bf16_f32 v127, v126, v127
	v_cvt_pk_bf16_f32 v126, v124, v125
	v_cvt_pk_bf16_f32 v124, v128, v129
	v_cvt_pk_bf16_f32 v125, v130, v131
	s_and_saveexec_b64 s[0:1], s[42:43]
	v_mul_u32_u24_e32 v128, s2, v159
	v_lshlrev_b32_e32 v129, v180, v192
	v_add3_u32 v212, v128, v129, v181
	v_lshl_add_u64 v[128:129], v[212:213], 1, s[52:53]
	global_store_dwordx4 v[128:129], v[124:127], off nt
	s_nop 1
	s_or_b64 exec, exec, s[0:1]
	v_cvt_pk_bf16_f32 v115, v114, v115
	v_cvt_pk_bf16_f32 v114, v112, v113
	v_cvt_pk_bf16_f32 v112, v116, v117
	v_cvt_pk_bf16_f32 v113, v118, v119
	s_and_saveexec_b64 s[0:1], s[44:45]
	v_mul_u32_u24_e32 v116, s2, v158
	v_lshlrev_b32_e32 v117, v145, v192
	v_add3_u32 v212, v116, v117, v172
	v_lshl_add_u64 v[116:117], v[212:213], 1, s[52:53]
	global_store_dwordx4 v[116:117], v[112:115], off nt
	s_nop 1
	s_or_b64 exec, exec, s[0:1]
	s_or_b32 s2, s4, 2
	v_cvt_pk_bf16_f32 v107, v106, v107
	v_cvt_pk_bf16_f32 v106, v104, v105
	v_cvt_pk_bf16_f32 v104, v108, v109
	v_cvt_pk_bf16_f32 v105, v110, v111
	s_and_saveexec_b64 s[0:1], s[42:43]
	v_mul_u32_u24_e32 v108, s2, v159
	v_lshl_or_b32 v108, v192, v180, v108
	v_add_u32_e32 v212, v108, v181
	v_lshl_add_u64 v[108:109], v[212:213], 1, s[52:53]
	global_store_dwordx4 v[108:109], v[104:107], off nt
	s_nop 1
	s_or_b64 exec, exec, s[0:1]
	v_cvt_pk_bf16_f32 v95, v94, v95
	v_cvt_pk_bf16_f32 v94, v92, v93
	v_cvt_pk_bf16_f32 v92, v96, v97
	v_cvt_pk_bf16_f32 v93, v98, v99
	s_and_saveexec_b64 s[0:1], s[44:45]
	v_mul_u32_u24_e32 v96, s2, v158
	v_lshl_or_b32 v96, v192, v145, v96
	v_add_u32_e32 v212, v96, v172
	v_lshl_add_u64 v[96:97], v[212:213], 1, s[52:53]
	global_store_dwordx4 v[96:97], v[92:95], off nt
	s_nop 1
	s_or_b64 exec, exec, s[0:1]
	s_or_b32 s2, s4, 3
	v_cvt_pk_bf16_f32 v87, v86, v87
	v_cvt_pk_bf16_f32 v86, v84, v85
	v_cvt_pk_bf16_f32 v84, v88, v89
	v_cvt_pk_bf16_f32 v85, v90, v91
	s_and_saveexec_b64 s[0:1], s[42:43]
	v_mul_u32_u24_e32 v88, s2, v159
	v_lshlrev_b32_e32 v89, v180, v192
	v_add3_u32 v212, v88, v89, v181
	v_lshl_add_u64 v[88:89], v[212:213], 1, s[52:53]
	global_store_dwordx4 v[88:89], v[84:87], off nt
	s_nop 1
	s_or_b64 exec, exec, s[0:1]
	v_cvt_pk_bf16_f32 v75, v74, v75
	v_cvt_pk_bf16_f32 v74, v72, v73
	v_cvt_pk_bf16_f32 v72, v76, v77
	v_cvt_pk_bf16_f32 v73, v78, v79
	s_and_saveexec_b64 s[0:1], s[44:45]
	v_mul_u32_u24_e32 v76, s2, v158
	v_lshlrev_b32_e32 v77, v145, v192
	v_add3_u32 v212, v76, v77, v172
	v_lshl_add_u64 v[76:77], v[212:213], 1, s[52:53]
	global_store_dwordx4 v[76:77], v[72:75], off nt
	s_nop 1
	s_or_b64 exec, exec, s[0:1]
	s_mov_b64 s[0:1], -1
	s_addk_i32 s8, 0x80
	s_lshr_b32 s0, s8, 4
	s_and_b32 s2, s0, 0xfc
	v_cvt_pk_bf16_f32 v67, v66, v67
	v_cvt_pk_bf16_f32 v66, v64, v65
	v_cvt_pk_bf16_f32 v64, v68, v69
	v_cvt_pk_bf16_f32 v65, v70, v71
	s_and_saveexec_b64 s[0:1], s[42:43]
	v_mul_u32_u24_e32 v68, s2, v159
	v_lshl_or_b32 v68, v192, v180, v68
	v_add_u32_e32 v212, v68, v181
	v_lshl_add_u64 v[68:69], v[212:213], 1, s[52:53]
	global_store_dwordx4 v[68:69], v[64:67], off nt
	s_nop 1
	s_or_b64 exec, exec, s[0:1]
	v_cvt_pk_bf16_f32 v55, v54, v55
	v_cvt_pk_bf16_f32 v54, v52, v53
	v_cvt_pk_bf16_f32 v52, v56, v57
	v_cvt_pk_bf16_f32 v53, v58, v59
	s_and_saveexec_b64 s[0:1], s[44:45]
	v_mul_u32_u24_e32 v56, s2, v158
	v_lshl_or_b32 v56, v192, v145, v56
	v_add_u32_e32 v212, v56, v172
	v_lshl_add_u64 v[56:57], v[212:213], 1, s[52:53]
	global_store_dwordx4 v[56:57], v[52:55], off nt
	s_nop 1
	s_or_b64 exec, exec, s[0:1]
	s_or_b32 s4, s2, 1
	v_cvt_pk_bf16_f32 v47, v46, v47
	v_cvt_pk_bf16_f32 v46, v44, v45
	v_cvt_pk_bf16_f32 v44, v48, v49
	v_cvt_pk_bf16_f32 v45, v50, v51
	s_and_saveexec_b64 s[0:1], s[42:43]
	v_mul_u32_u24_e32 v48, s4, v159
	v_lshlrev_b32_e32 v49, v180, v192
	v_add3_u32 v212, v48, v49, v181
	v_lshl_add_u64 v[48:49], v[212:213], 1, s[52:53]
	global_store_dwordx4 v[48:49], v[44:47], off nt
	s_nop 1
	s_or_b64 exec, exec, s[0:1]
	v_cvt_pk_bf16_f32 v35, v34, v35
	v_cvt_pk_bf16_f32 v34, v32, v33
	v_cvt_pk_bf16_f32 v32, v36, v37
	v_cvt_pk_bf16_f32 v33, v38, v39
	s_and_saveexec_b64 s[0:1], s[44:45]
	v_mul_u32_u24_e32 v36, s4, v158
	v_lshlrev_b32_e32 v37, v145, v192
	v_add3_u32 v212, v36, v37, v172
	v_lshl_add_u64 v[36:37], v[212:213], 1, s[52:53]
	global_store_dwordx4 v[36:37], v[32:35], off nt
	s_nop 1
	s_or_b64 exec, exec, s[0:1]
	s_or_b32 s4, s2, 2
	v_cvt_pk_bf16_f32 v27, v26, v27
	v_cvt_pk_bf16_f32 v26, v24, v25
	v_cvt_pk_bf16_f32 v24, v28, v29
	v_cvt_pk_bf16_f32 v25, v30, v31
	s_and_saveexec_b64 s[0:1], s[42:43]
	v_mul_u32_u24_e32 v28, s4, v159
	v_lshl_or_b32 v28, v192, v180, v28
	v_add_u32_e32 v212, v28, v181
	v_lshl_add_u64 v[28:29], v[212:213], 1, s[52:53]
	global_store_dwordx4 v[28:29], v[24:27], off nt
	s_nop 1
	s_or_b64 exec, exec, s[0:1]
	v_cvt_pk_bf16_f32 v19, v18, v19
	v_cvt_pk_bf16_f32 v18, v16, v17
	v_cvt_pk_bf16_f32 v16, v20, v21
	v_cvt_pk_bf16_f32 v17, v22, v23
	s_and_saveexec_b64 s[0:1], s[44:45]
	v_mul_u32_u24_e32 v20, s4, v158
	v_lshl_or_b32 v20, v192, v145, v20
	v_add_u32_e32 v212, v20, v172
	v_lshl_add_u64 v[20:21], v[212:213], 1, s[52:53]
	global_store_dwordx4 v[20:21], v[16:19], off nt
	s_nop 1
	s_or_b64 exec, exec, s[0:1]
	s_or_b32 s2, s2, 3
	v_cvt_pk_bf16_f32 v11, v10, v11
	v_cvt_pk_bf16_f32 v10, v8, v9
	v_cvt_pk_bf16_f32 v8, v12, v13
	v_cvt_pk_bf16_f32 v9, v14, v15
	s_and_saveexec_b64 s[0:1], s[42:43]
	v_mul_u32_u24_e32 v12, s2, v159
	v_lshlrev_b32_e32 v13, v180, v192
	v_add3_u32 v212, v12, v13, v181
	v_lshl_add_u64 v[12:13], v[212:213], 1, s[52:53]
	global_store_dwordx4 v[12:13], v[8:11], off nt
	s_nop 1
	s_or_b64 exec, exec, s[0:1]
	s_and_b64 vcc, exec, s[38:39]
	v_cvt_pk_bf16_f32 v3, v2, v3
	v_cvt_pk_bf16_f32 v2, v0, v1
	v_cvt_pk_bf16_f32 v0, v4, v5
	v_cvt_pk_bf16_f32 v1, v6, v7
	s_and_saveexec_b64 s[0:1], s[44:45]
	v_mul_u32_u24_e32 v4, s2, v158
	v_lshlrev_b32_e32 v5, v145, v192
	v_add3_u32 v212, v4, v5, v172
	v_lshl_add_u64 v[4:5], v[212:213], 1, s[52:53]
	global_store_dwordx4 v[4:5], v[0:3], off nt
	s_nop 1
	s_branch .LBB0_464

.Lepiz_m2:
	v_cndmask_b32_e64 v172, 0, 1, s[80:81]
	v_cmp_ne_u32_e64 s[40:41], 1, v172
	s_mov_b64 s[4:5], -1
	v_cndmask_b32_e64 v159, 0, 1, s[0:1]
	v_cmp_ne_u32_e64 s[38:39], 1, v159
	v_mul_f32_e32 v156, 0xbfb8aa3b, v148
	v_exp_f32_e32 v156, v156
	s_nop 0
	v_add_f32_e32 v156, 1.0, v156
	v_rcp_f32_e32 v178, v156
	v_mul_f32_e32 v156, 0xbfb8aa3b, v144
	v_exp_f32_e32 v156, v156
	s_nop 0
	v_add_f32_e32 v156, 1.0, v156
	v_rcp_f32_e32 v180, v156
	v_mul_f32_e32 v156, 0xbfb8aa3b, v149
	v_exp_f32_e32 v156, v156
	s_nop 0
	v_add_f32_e32 v156, 1.0, v156
	v_rcp_f32_e32 v179, v156
	v_mul_f32_e32 v156, 0xbfb8aa3b, v145
	v_exp_f32_e32 v156, v156
	v_pk_mul_f32 v[148:149], v[148:149], v[178:179]
	v_add_f32_e32 v156, 1.0, v156
	v_rcp_f32_e32 v181, v156
	v_mul_f32_e32 v156, 0xbfb8aa3b, v150
	v_exp_f32_e32 v156, v156
	v_pk_mul_f32 v[144:145], v[144:145], v[180:181]
	v_add_f32_e32 v156, 1.0, v156
	v_rcp_f32_e32 v182, v156
	v_mul_f32_e32 v156, 0xbfb8aa3b, v146
	v_exp_f32_e32 v156, v156
	s_nop 0
	v_add_f32_e32 v156, 1.0, v156
	v_rcp_f32_e32 v184, v156
	v_mul_f32_e32 v156, 0xbfb8aa3b, v151
	v_exp_f32_e32 v156, v156
	s_nop 0
	v_add_f32_e32 v156, 1.0, v156
	v_rcp_f32_e32 v183, v156
	v_mul_f32_e32 v156, 0xbfb8aa3b, v147
	v_exp_f32_e32 v156, v156
	v_pk_mul_f32 v[150:151], v[150:151], v[182:183]
	v_add_f32_e32 v156, 1.0, v156
	v_rcp_f32_e32 v185, v156
	s_nop 0
	v_pk_mul_f32 v[146:147], v[146:147], v[184:185]
	v_mov_b32_e32 v156, v148
	v_mov_b32_e32 v179, v149
	v_mov_b32_e32 v180, v150
	v_mov_b32_e32 v182, v151
	v_mov_b32_e32 v178, v144
	v_mov_b32_e32 v185, v145
	v_mov_b32_e32 v186, v146
	v_mov_b32_e32 v188, v147
	s_lshr_b32 s0, s8, 4
	s_and_b32 s4, s0, 0xfc
	s_ashr_i32 s0, s2, 31
	s_lshr_b32 s0, s0, 28
	s_add_i32 s0, s2, s0
	s_ashr_i32 s13, s0, 4
	v_add_u32_e32 v144, v204, v201
	s_movk_i32 s0, 0x300
	v_mul_lo_u32 v144, v144, s0
	v_sub_u32_e32 v144, v193, v144
	v_cndmask_b32_e64 v146, v203, v144, s[42:43]
	v_lshrrev_b32_e32 v144, 7, v146
	v_mad_u64_u32 v[144:145], s[0:1], v202, s13, v[144:145]
	v_lshlrev_b32_e32 v145, 4, v146
	v_lshl_add_u32 v144, v144, 19, v200
	v_and_b32_e32 v145, 0x600, v145
	v_and_b32_e32 v146, 31, v146
	v_or3_b32 v146, v144, v145, v146
	v_add_u32_e32 v144, 0xfffff200, v193
	v_mul_hi_i32 v145, v144, s6
	v_lshrrev_b32_e32 v147, 31, v145
	v_ashrrev_i32_e32 v145, 6, v145
	v_add_u32_e32 v145, v145, v147
	v_mul_i32_i24_e32 v147, 0x180, v145
	v_sub_u32_e32 v144, v144, v147
	v_mul_i32_i24_e32 v147, 0x2aab, v144
	v_mov_b32_e32 v148, 4
	v_ashrrev_i16_sdwa v148, v148, v147 dst_sel:DWORD dst_unused:UNUSED_PAD src0_sel:DWORD src1_sel:WORD_1
	v_lshrrev_b32_e32 v147, 31, v147
	v_add_u16_e32 v147, v148, v147
	v_mul_lo_u16_e32 v148, 0x60, v147
	v_sub_u16_e32 v144, v144, v148
	s_lshl_b32 s5, s13, 2
	v_bfe_i32 v148, v144, 0, 16
	v_mul_i32_i24_e32 v144, 0x600000, v145
	v_and_or_b32 v144, v148, 31, v144
	v_add_u32_e32 v145, s5, v147
	s_mov_b32 s0, 0x60000
	v_lshlrev_b32_e32 v147, 4, v148
	v_mad_u64_u32 v[144:145], s[0:1], v145, s0, v[144:145]
	v_and_b32_e32 v147, 0xfffffe00, v147
	s_mov_b32 s0, 0x3800000
	v_add3_u32 v147, v144, v147, s0
	v_add_u32_e32 v144, 0xffffef00, v193
	v_mul_hi_i32 v145, v144, s6
	v_lshrrev_b32_e32 v148, 31, v145
	v_ashrrev_i32_e32 v145, 7, v145
	v_add_u32_e32 v145, v145, v148
	v_mul_i32_i24_e32 v148, 0x300, v145
	v_sub_u32_e32 v144, v144, v148
	v_mul_i32_i24_e32 v148, 0x2aab, v144
	v_mov_b32_e32 v149, 5
	v_ashrrev_i16_sdwa v149, v149, v148 dst_sel:DWORD dst_unused:UNUSED_PAD src0_sel:DWORD src1_sel:WORD_1
	v_lshrrev_b32_e32 v148, 31, v148
	v_add_u16_e32 v148, v149, v148
	v_mul_lo_u16_e32 v149, 0xc0, v148
	v_sub_u16_e32 v144, v144, v149
	s_mov_b32 s0, 0xc00000
	v_bfe_i32 v149, v144, 0, 16
	v_mul_lo_u32 v144, v145, s0
	v_and_or_b32 v144, v149, 31, v144
	v_add_u32_e32 v145, s5, v148
	s_mov_b32 s0, 0xc0000
	v_lshlrev_b32_e32 v148, 4, v149
	v_mad_u64_u32 v[144:145], s[0:1], v145, s0, v[144:145]
	v_and_b32_e32 v148, 0xfffffe00, v148
	s_mov_b32 s0, 0x4400000
	v_add3_u32 v144, v144, v148, s0
	s_movk_i32 s0, 0xe00
	s_lshl_b32 s2, s13, 16
	v_cmp_gt_i32_e32 vcc, s0, v193
	s_movk_i32 s0, 0x1710
	s_add_i32 s2, s2, 0x5bfe900
	v_cmp_gt_u32_e64 s[42:43], s0, v193
	s_movk_i32 s0, 0x1700
	v_add_u32_e32 v145, s2, v193
	v_cndmask_b32_e64 v149, 0, v237, s[42:43]
	v_cmp_gt_i32_e64 s[46:47], s0, v193
	s_movk_i32 s0, 0x1100
	v_cndmask_b32_e32 v148, v236, v218, vcc
	v_cndmask_b32_e64 v149, v149, v239, s[46:47]
	v_cmp_gt_i32_e64 s[42:43], s0, v193
	v_cndmask_b32_e64 v144, v145, v144, s[46:47]
	s_nop 0
	v_cndmask_b32_e64 v159, v149, v148, s[42:43]
	v_cndmask_b32_e64 v144, v144, v147, s[42:43]
	v_cndmask_b32_e32 v181, v144, v146, vcc
	v_cvt_pk_bf16_f32 v144, v156, v179
	v_cvt_pk_bf16_f32 v145, v180, v182
	v_cmp_ne_u32_e64 s[42:43], 0, v159
	v_cndmask_b32_e64 v180, 4, 5, s[46:47]
	v_cvt_pk_bf16_f32 v146, v178, v185
	v_cvt_pk_bf16_f32 v147, v186, v188
	s_and_saveexec_b64 s[0:1], s[42:43]
	v_mul_u32_u24_e32 v148, s4, v159
	v_lshl_or_b32 v148, v192, v180, v148
	v_add_u32_e32 v212, v148, v181
	v_lshl_add_u64 v[148:149], v[212:213], 1, s[52:53]
	global_store_dwordx4 v[148:149], v[144:147], off nt
	s_nop 1
	s_or_b64 exec, exec, s[0:1]
	s_mov_b64 s[0:1], -1
	v_mul_f32_e32 v145, 0xbfb8aa3b, v132
	v_exp_f32_e32 v145, v145
	v_mul_f32_e32 v144, 0xbfb8aa3b, v136
	v_exp_f32_e32 v144, v144
	v_mul_f32_e32 v149, 0xbfb8aa3b, v134
	v_add_f32_e32 v145, 1.0, v145
	v_rcp_f32_e32 v146, v145
	v_mul_f32_e32 v145, 0xbfb8aa3b, v137
	v_exp_f32_e32 v145, v145
	v_add_f32_e32 v144, 1.0, v144
	v_exp_f32_e32 v149, v149
	v_rcp_f32_e32 v144, v144
	v_add_f32_e32 v145, 1.0, v145
	v_rcp_f32_e32 v145, v145
	v_add_f32_e32 v149, 1.0, v149
	v_mul_f32_e32 v147, 0xbfb8aa3b, v133
	v_mul_f32_e32 v148, 0xbfb8aa3b, v138
	v_rcp_f32_e32 v150, v149
	v_mul_f32_e32 v149, 0xbfb8aa3b, v139
	v_pk_mul_f32 v[136:137], v[136:137], v[144:145]
	v_mul_f32_e32 v144, 0xbfb8aa3b, v135
	v_exp_f32_e32 v147, v147
	v_exp_f32_e32 v148, v148
	v_exp_f32_e32 v149, v149
	v_exp_f32_e32 v144, v144
	v_add_f32_e32 v147, 1.0, v147
	v_add_f32_e32 v148, 1.0, v148
	v_add_f32_e32 v149, 1.0, v149
	v_add_f32_e32 v144, 1.0, v144
	v_rcp_f32_e32 v147, v147
	v_rcp_f32_e32 v148, v148
	v_rcp_f32_e32 v149, v149
	v_rcp_f32_e32 v151, v144
	v_pk_mul_f32 v[132:133], v[132:133], v[146:147]
	v_pk_mul_f32 v[138:139], v[138:139], v[148:149]
	v_pk_mul_f32 v[134:135], v[134:135], v[150:151]
	v_mov_b32_e32 v144, v136
	v_mov_b32_e32 v145, v137
	v_mov_b32_e32 v146, v138
	v_mov_b32_e32 v148, v139
	v_mov_b32_e32 v147, v132
	v_mov_b32_e32 v151, v133
	v_mov_b32_e32 v178, v134
	v_mov_b32_e32 v156, v135
	v_add_u32_e32 v132, v198, v197
	s_movk_i32 s0, 0x300
	v_mul_lo_u32 v132, v132, s0
	v_sub_u32_e32 v132, v194, v132
	v_cndmask_b32_e64 v134, v199, v132, s[44:45]
	v_lshrrev_b32_e32 v132, 7, v134
	v_mad_u64_u32 v[132:133], s[0:1], v195, s13, v[132:133]
	v_lshlrev_b32_e32 v133, 4, v134
	v_lshl_add_u32 v132, v132, 19, v196
	v_and_b32_e32 v133, 0x600, v133
	v_and_b32_e32 v134, 31, v134
	v_or3_b32 v134, v132, v133, v134
	v_add_u32_e32 v132, 0xfffff280, v193
	v_mul_hi_i32 v133, v132, s6
	v_lshrrev_b32_e32 v135, 31, v133
	v_ashrrev_i32_e32 v133, 6, v133
	v_add_u32_e32 v133, v133, v135
	v_mul_i32_i24_e32 v135, 0x180, v133
	v_sub_u32_e32 v132, v132, v135
	v_mul_i32_i24_e32 v135, 0x2aab, v132
	v_lshrrev_b32_e32 v136, 31, v135
	v_ashrrev_i32_e32 v135, 20, v135
	v_add_u16_e32 v135, v135, v136
	v_mul_lo_u16_e32 v136, 0x60, v135
	v_sub_u16_e32 v132, v132, v136
	v_bfe_i32 v136, v132, 0, 16
	v_mul_i32_i24_e32 v132, 0x600000, v133
	v_and_or_b32 v132, v136, 31, v132
	v_add_u32_e32 v133, s5, v135
	s_mov_b32 s0, 0x60000
	v_lshlrev_b32_e32 v135, 4, v136
	v_mad_u64_u32 v[132:133], s[0:1], v133, s0, v[132:133]
	v_and_b32_e32 v135, 0xfffffe00, v135
	s_mov_b32 s0, 0x3800000
	v_add3_u32 v135, v132, v135, s0
	v_add_u32_e32 v132, 0xffffef80, v193
	v_mul_hi_i32 v133, v132, s6
	v_lshrrev_b32_e32 v136, 31, v133
	v_ashrrev_i32_e32 v133, 7, v133
	v_add_u32_e32 v133, v133, v136
	v_mul_i32_i24_e32 v136, 0x300, v133
	v_sub_u32_e32 v132, v132, v136
	v_mul_i32_i24_e32 v136, 0x2aab, v132
	v_lshrrev_b32_e32 v137, 31, v136
	v_ashrrev_i32_e32 v136, 21, v136
	v_add_u16_e32 v136, v136, v137
	v_mul_lo_u16_e32 v137, 0xc0, v136
	v_sub_u16_e32 v132, v132, v137
	s_mov_b32 s0, 0xc00000
	v_bfe_i32 v137, v132, 0, 16
	v_mul_lo_u32 v132, v133, s0
	v_and_or_b32 v132, v137, 31, v132
	v_add_u32_e32 v133, s5, v136
	s_mov_b32 s0, 0xc0000
	v_lshlrev_b32_e32 v136, 4, v137
	v_mad_u64_u32 v[132:133], s[0:1], v133, s0, v[132:133]
	v_and_b32_e32 v136, 0xfffffe00, v136
	s_mov_b32 s0, 0x4400000
	v_add3_u32 v132, v132, v136, s0
	s_movk_i32 s0, 0xd80
	v_cmp_gt_i32_e32 vcc, s0, v193
	s_movk_i32 s0, 0x1710
	v_cmp_gt_u32_e64 s[44:45], s0, v194
	s_movk_i32 s0, 0x1680
	v_add_u32_e32 v133, s2, v194
	v_cndmask_b32_e64 v137, 0, v237, s[44:45]
	v_cmp_gt_i32_e64 s[46:47], s0, v193
	s_movk_i32 s0, 0x1080
	v_cndmask_b32_e32 v136, v236, v218, vcc
	v_cndmask_b32_e64 v137, v137, v239, s[46:47]
	v_cmp_gt_i32_e64 s[44:45], s0, v193
	v_cndmask_b32_e64 v132, v133, v132, s[46:47]
	s_nop 0
	v_cndmask_b32_e64 v158, v137, v136, s[44:45]
	v_cndmask_b32_e64 v132, v132, v135, s[44:45]
	v_cndmask_b32_e32 v172, v132, v134, vcc
	v_cvt_pk_bf16_f32 v132, v144, v145
	v_cmp_ne_u32_e64 s[44:45], 0, v158
	v_cndmask_b32_e64 v145, 4, 5, s[46:47]
	v_cvt_pk_bf16_f32 v133, v146, v148
	v_cvt_pk_bf16_f32 v134, v147, v151
	v_cvt_pk_bf16_f32 v135, v178, v156
	s_and_saveexec_b64 s[0:1], s[44:45]
	v_mul_u32_u24_e32 v136, s4, v158
	v_lshl_or_b32 v136, v192, v145, v136
	v_add_u32_e32 v212, v136, v172
	v_lshl_add_u64 v[136:137], v[212:213], 1, s[52:53]
	global_store_dwordx4 v[136:137], v[132:135], off nt
	s_nop 1
	s_or_b64 exec, exec, s[0:1]
	v_mul_f32_e32 v134, 0xbfb8aa3b, v128
	v_exp_f32_e32 v134, v134
	s_nop 0
	v_add_f32_e32 v134, 1.0, v134
	v_rcp_f32_e32 v146, v134
	v_mul_f32_e32 v134, 0xbfb8aa3b, v124
	v_exp_f32_e32 v134, v134
	s_nop 0
	v_add_f32_e32 v134, 1.0, v134
	v_rcp_f32_e32 v148, v134
	v_mul_f32_e32 v134, 0xbfb8aa3b, v129
	v_exp_f32_e32 v134, v134
	s_nop 0
	v_add_f32_e32 v134, 1.0, v134
	v_rcp_f32_e32 v147, v134
	v_mul_f32_e32 v134, 0xbfb8aa3b, v125
	v_exp_f32_e32 v134, v134
	v_pk_mul_f32 v[128:129], v[128:129], v[146:147]
	v_add_f32_e32 v134, 1.0, v134
	v_rcp_f32_e32 v149, v134
	v_mul_f32_e32 v134, 0xbfb8aa3b, v130
	v_exp_f32_e32 v134, v134
	v_pk_mul_f32 v[124:125], v[124:125], v[148:149]
	v_add_f32_e32 v134, 1.0, v134
	v_rcp_f32_e32 v150, v134
	v_mul_f32_e32 v134, 0xbfb8aa3b, v126
	v_exp_f32_e32 v134, v134
	s_nop 0
	v_add_f32_e32 v134, 1.0, v134
	v_rcp_f32_e32 v152, v134
	v_mul_f32_e32 v134, 0xbfb8aa3b, v131
	v_exp_f32_e32 v134, v134
	s_nop 0
	v_add_f32_e32 v134, 1.0, v134
	v_rcp_f32_e32 v151, v134
	v_mul_f32_e32 v134, 0xbfb8aa3b, v127
	v_exp_f32_e32 v134, v134
	v_pk_mul_f32 v[130:131], v[130:131], v[150:151]
	v_add_f32_e32 v134, 1.0, v134
	v_rcp_f32_e32 v153, v134
	s_nop 0
	v_pk_mul_f32 v[126:127], v[126:127], v[152:153]
	s_or_b32 s2, s4, 1
	v_cvt_pk_bf16_f32 v127, v126, v127
	v_cvt_pk_bf16_f32 v126, v124, v125
	v_cvt_pk_bf16_f32 v124, v128, v129
	v_cvt_pk_bf16_f32 v125, v130, v131
	s_and_saveexec_b64 s[0:1], s[42:43]
	v_mul_u32_u24_e32 v128, s2, v159
	v_lshlrev_b32_e32 v129, v180, v192
	v_add3_u32 v212, v128, v129, v181
	v_lshl_add_u64 v[128:129], v[212:213], 1, s[52:53]
	global_store_dwordx4 v[128:129], v[124:127], off nt
	s_nop 1
	s_or_b64 exec, exec, s[0:1]
	v_mul_f32_e32 v125, 0xbfb8aa3b, v112
	v_exp_f32_e32 v125, v125
	v_mul_f32_e32 v124, 0xbfb8aa3b, v116
	v_exp_f32_e32 v124, v124
	v_mul_f32_e32 v129, 0xbfb8aa3b, v114
	v_add_f32_e32 v125, 1.0, v125
	v_rcp_f32_e32 v126, v125
	v_mul_f32_e32 v125, 0xbfb8aa3b, v117
	v_exp_f32_e32 v125, v125
	v_add_f32_e32 v124, 1.0, v124
	v_exp_f32_e32 v129, v129
	v_rcp_f32_e32 v124, v124
	v_add_f32_e32 v125, 1.0, v125
	v_rcp_f32_e32 v125, v125
	v_add_f32_e32 v129, 1.0, v129
	v_mul_f32_e32 v127, 0xbfb8aa3b, v113
	v_mul_f32_e32 v128, 0xbfb8aa3b, v118
	v_rcp_f32_e32 v130, v129
	v_mul_f32_e32 v129, 0xbfb8aa3b, v119
	v_pk_mul_f32 v[116:117], v[116:117], v[124:125]
	v_mul_f32_e32 v124, 0xbfb8aa3b, v115
	v_exp_f32_e32 v127, v127
	v_exp_f32_e32 v128, v128
	v_exp_f32_e32 v129, v129
	v_exp_f32_e32 v124, v124
	v_add_f32_e32 v127, 1.0, v127
	v_add_f32_e32 v128, 1.0, v128
	v_add_f32_e32 v129, 1.0, v129
	v_add_f32_e32 v124, 1.0, v124
	v_rcp_f32_e32 v127, v127
	v_rcp_f32_e32 v128, v128
	v_rcp_f32_e32 v129, v129
	v_rcp_f32_e32 v131, v124
	v_pk_mul_f32 v[112:113], v[112:113], v[126:127]
	v_pk_mul_f32 v[118:119], v[118:119], v[128:129]
	v_pk_mul_f32 v[114:115], v[114:115], v[130:131]
	v_cvt_pk_bf16_f32 v115, v114, v115
	v_cvt_pk_bf16_f32 v114, v112, v113
	v_cvt_pk_bf16_f32 v112, v116, v117
	v_cvt_pk_bf16_f32 v113, v118, v119
	s_and_saveexec_b64 s[0:1], s[44:45]
	v_mul_u32_u24_e32 v116, s2, v158
	v_lshlrev_b32_e32 v117, v145, v192
	v_add3_u32 v212, v116, v117, v172
	v_lshl_add_u64 v[116:117], v[212:213], 1, s[52:53]
	global_store_dwordx4 v[116:117], v[112:115], off nt
	s_nop 1
	s_or_b64 exec, exec, s[0:1]
	v_mul_f32_e32 v114, 0xbfb8aa3b, v108
	v_exp_f32_e32 v114, v114
	s_nop 0
	v_add_f32_e32 v114, 1.0, v114
	v_rcp_f32_e32 v126, v114
	v_mul_f32_e32 v114, 0xbfb8aa3b, v104
	v_exp_f32_e32 v114, v114
	s_nop 0
	v_add_f32_e32 v114, 1.0, v114
	v_rcp_f32_e32 v128, v114
	v_mul_f32_e32 v114, 0xbfb8aa3b, v109
	v_exp_f32_e32 v114, v114
	s_nop 0
	v_add_f32_e32 v114, 1.0, v114
	v_rcp_f32_e32 v127, v114
	v_mul_f32_e32 v114, 0xbfb8aa3b, v105
	v_exp_f32_e32 v114, v114
	v_pk_mul_f32 v[108:109], v[108:109], v[126:127]
	v_add_f32_e32 v114, 1.0, v114
	v_rcp_f32_e32 v129, v114
	v_mul_f32_e32 v114, 0xbfb8aa3b, v110
	v_exp_f32_e32 v114, v114
	v_pk_mul_f32 v[104:105], v[104:105], v[128:129]
	v_add_f32_e32 v114, 1.0, v114
	v_rcp_f32_e32 v130, v114
	v_mul_f32_e32 v114, 0xbfb8aa3b, v106
	v_exp_f32_e32 v114, v114
	s_nop 0
	v_add_f32_e32 v114, 1.0, v114
	v_rcp_f32_e32 v132, v114
	v_mul_f32_e32 v114, 0xbfb8aa3b, v111
	v_exp_f32_e32 v114, v114
	s_nop 0
	v_add_f32_e32 v114, 1.0, v114
	v_rcp_f32_e32 v131, v114
	v_mul_f32_e32 v114, 0xbfb8aa3b, v107
	v_exp_f32_e32 v114, v114
	v_pk_mul_f32 v[110:111], v[110:111], v[130:131]
	v_add_f32_e32 v114, 1.0, v114
	v_rcp_f32_e32 v133, v114
	s_nop 0
	v_pk_mul_f32 v[106:107], v[106:107], v[132:133]
	s_or_b32 s2, s4, 2
	v_cvt_pk_bf16_f32 v107, v106, v107
	v_cvt_pk_bf16_f32 v106, v104, v105
	v_cvt_pk_bf16_f32 v104, v108, v109
	v_cvt_pk_bf16_f32 v105, v110, v111
	s_and_saveexec_b64 s[0:1], s[42:43]
	v_mul_u32_u24_e32 v108, s2, v159
	v_lshl_or_b32 v108, v192, v180, v108
	v_add_u32_e32 v212, v108, v181
	v_lshl_add_u64 v[108:109], v[212:213], 1, s[52:53]
	global_store_dwordx4 v[108:109], v[104:107], off nt
	s_nop 1
	s_or_b64 exec, exec, s[0:1]
	v_mul_f32_e32 v105, 0xbfb8aa3b, v92
	v_exp_f32_e32 v105, v105
	v_mul_f32_e32 v104, 0xbfb8aa3b, v96
	v_exp_f32_e32 v104, v104
	v_mul_f32_e32 v109, 0xbfb8aa3b, v94
	v_add_f32_e32 v105, 1.0, v105
	v_rcp_f32_e32 v106, v105
	v_mul_f32_e32 v105, 0xbfb8aa3b, v97
	v_exp_f32_e32 v105, v105
	v_add_f32_e32 v104, 1.0, v104
	v_exp_f32_e32 v109, v109
	v_rcp_f32_e32 v104, v104
	v_add_f32_e32 v105, 1.0, v105
	v_rcp_f32_e32 v105, v105
	v_add_f32_e32 v109, 1.0, v109
	v_mul_f32_e32 v107, 0xbfb8aa3b, v93
	v_mul_f32_e32 v108, 0xbfb8aa3b, v98
	v_rcp_f32_e32 v110, v109
	v_mul_f32_e32 v109, 0xbfb8aa3b, v99
	v_pk_mul_f32 v[96:97], v[96:97], v[104:105]
	v_mul_f32_e32 v104, 0xbfb8aa3b, v95
	v_exp_f32_e32 v107, v107
	v_exp_f32_e32 v108, v108
	v_exp_f32_e32 v109, v109
	v_exp_f32_e32 v104, v104
	v_add_f32_e32 v107, 1.0, v107
	v_add_f32_e32 v108, 1.0, v108
	v_add_f32_e32 v109, 1.0, v109
	v_add_f32_e32 v104, 1.0, v104
	v_rcp_f32_e32 v107, v107
	v_rcp_f32_e32 v108, v108
	v_rcp_f32_e32 v109, v109
	v_rcp_f32_e32 v111, v104
	v_pk_mul_f32 v[92:93], v[92:93], v[106:107]
	v_pk_mul_f32 v[98:99], v[98:99], v[108:109]
	v_pk_mul_f32 v[94:95], v[94:95], v[110:111]
	v_cvt_pk_bf16_f32 v95, v94, v95
	v_cvt_pk_bf16_f32 v94, v92, v93
	v_cvt_pk_bf16_f32 v92, v96, v97
	v_cvt_pk_bf16_f32 v93, v98, v99
	s_and_saveexec_b64 s[0:1], s[44:45]
	v_mul_u32_u24_e32 v96, s2, v158
	v_lshl_or_b32 v96, v192, v145, v96
	v_add_u32_e32 v212, v96, v172
	v_lshl_add_u64 v[96:97], v[212:213], 1, s[52:53]
	global_store_dwordx4 v[96:97], v[92:95], off nt
	s_nop 1
	s_or_b64 exec, exec, s[0:1]
	v_mul_f32_e32 v94, 0xbfb8aa3b, v88
	v_exp_f32_e32 v94, v94
	s_nop 0
	v_add_f32_e32 v94, 1.0, v94
	v_rcp_f32_e32 v106, v94
	v_mul_f32_e32 v94, 0xbfb8aa3b, v84
	v_exp_f32_e32 v94, v94
	s_nop 0
	v_add_f32_e32 v94, 1.0, v94
	v_rcp_f32_e32 v108, v94
	v_mul_f32_e32 v94, 0xbfb8aa3b, v89
	v_exp_f32_e32 v94, v94
	s_nop 0
	v_add_f32_e32 v94, 1.0, v94
	v_rcp_f32_e32 v107, v94
	v_mul_f32_e32 v94, 0xbfb8aa3b, v85
	v_exp_f32_e32 v94, v94
	v_pk_mul_f32 v[88:89], v[88:89], v[106:107]
	v_add_f32_e32 v94, 1.0, v94
	v_rcp_f32_e32 v109, v94
	v_mul_f32_e32 v94, 0xbfb8aa3b, v90
	v_exp_f32_e32 v94, v94
	v_pk_mul_f32 v[84:85], v[84:85], v[108:109]
	v_add_f32_e32 v94, 1.0, v94
	v_rcp_f32_e32 v110, v94
	v_mul_f32_e32 v94, 0xbfb8aa3b, v86
	v_exp_f32_e32 v94, v94
	s_nop 0
	v_add_f32_e32 v94, 1.0, v94
	v_rcp_f32_e32 v112, v94
	v_mul_f32_e32 v94, 0xbfb8aa3b, v91
	v_exp_f32_e32 v94, v94
	s_nop 0
	v_add_f32_e32 v94, 1.0, v94
	v_rcp_f32_e32 v111, v94
	v_mul_f32_e32 v94, 0xbfb8aa3b, v87
	v_exp_f32_e32 v94, v94
	v_pk_mul_f32 v[90:91], v[90:91], v[110:111]
	v_add_f32_e32 v94, 1.0, v94
	v_rcp_f32_e32 v113, v94
	s_nop 0
	v_pk_mul_f32 v[86:87], v[86:87], v[112:113]
	s_or_b32 s2, s4, 3
	v_cvt_pk_bf16_f32 v87, v86, v87
	v_cvt_pk_bf16_f32 v86, v84, v85
	v_cvt_pk_bf16_f32 v84, v88, v89
	v_cvt_pk_bf16_f32 v85, v90, v91
	s_and_saveexec_b64 s[0:1], s[42:43]
	v_mul_u32_u24_e32 v88, s2, v159
	v_lshlrev_b32_e32 v89, v180, v192
	v_add3_u32 v212, v88, v89, v181
	v_lshl_add_u64 v[88:89], v[212:213], 1, s[52:53]
	global_store_dwordx4 v[88:89], v[84:87], off nt
	s_nop 1
	s_or_b64 exec, exec, s[0:1]
	v_mul_f32_e32 v85, 0xbfb8aa3b, v72
	v_exp_f32_e32 v85, v85
	v_mul_f32_e32 v84, 0xbfb8aa3b, v76
	v_exp_f32_e32 v84, v84
	v_mul_f32_e32 v89, 0xbfb8aa3b, v74
	v_add_f32_e32 v85, 1.0, v85
	v_rcp_f32_e32 v86, v85
	v_mul_f32_e32 v85, 0xbfb8aa3b, v77
	v_exp_f32_e32 v85, v85
	v_add_f32_e32 v84, 1.0, v84
	v_exp_f32_e32 v89, v89
	v_rcp_f32_e32 v84, v84
	v_add_f32_e32 v85, 1.0, v85
	v_rcp_f32_e32 v85, v85
	v_add_f32_e32 v89, 1.0, v89
	v_mul_f32_e32 v87, 0xbfb8aa3b, v73
	v_mul_f32_e32 v88, 0xbfb8aa3b, v78
	v_rcp_f32_e32 v90, v89
	v_mul_f32_e32 v89, 0xbfb8aa3b, v79
	v_pk_mul_f32 v[76:77], v[76:77], v[84:85]
	v_mul_f32_e32 v84, 0xbfb8aa3b, v75
	v_exp_f32_e32 v87, v87
	v_exp_f32_e32 v88, v88
	v_exp_f32_e32 v89, v89
	v_exp_f32_e32 v84, v84
	v_add_f32_e32 v87, 1.0, v87
	v_add_f32_e32 v88, 1.0, v88
	v_add_f32_e32 v89, 1.0, v89
	v_add_f32_e32 v84, 1.0, v84
	v_rcp_f32_e32 v87, v87
	v_rcp_f32_e32 v88, v88
	v_rcp_f32_e32 v89, v89
	v_rcp_f32_e32 v91, v84
	v_pk_mul_f32 v[72:73], v[72:73], v[86:87]
	v_pk_mul_f32 v[78:79], v[78:79], v[88:89]
	v_pk_mul_f32 v[74:75], v[74:75], v[90:91]
	v_cvt_pk_bf16_f32 v75, v74, v75
	v_cvt_pk_bf16_f32 v74, v72, v73
	v_cvt_pk_bf16_f32 v72, v76, v77
	v_cvt_pk_bf16_f32 v73, v78, v79
	s_and_saveexec_b64 s[0:1], s[44:45]
	v_mul_u32_u24_e32 v76, s2, v158
	v_lshlrev_b32_e32 v77, v145, v192
	v_add3_u32 v212, v76, v77, v172
	v_lshl_add_u64 v[76:77], v[212:213], 1, s[52:53]
	global_store_dwordx4 v[76:77], v[72:75], off nt
	s_nop 1
	s_or_b64 exec, exec, s[0:1]
	s_mov_b64 s[0:1], -1
	v_mul_f32_e32 v74, 0xbfb8aa3b, v68
	v_exp_f32_e32 v74, v74
	s_nop 0
	v_add_f32_e32 v74, 1.0, v74
	v_rcp_f32_e32 v86, v74
	v_mul_f32_e32 v74, 0xbfb8aa3b, v64
	v_exp_f32_e32 v74, v74
	s_nop 0
	v_add_f32_e32 v74, 1.0, v74
	v_rcp_f32_e32 v88, v74
	v_mul_f32_e32 v74, 0xbfb8aa3b, v69
	v_exp_f32_e32 v74, v74
	s_nop 0
	v_add_f32_e32 v74, 1.0, v74
	v_rcp_f32_e32 v87, v74
	v_mul_f32_e32 v74, 0xbfb8aa3b, v65
	v_exp_f32_e32 v74, v74
	v_pk_mul_f32 v[68:69], v[68:69], v[86:87]
	v_add_f32_e32 v74, 1.0, v74
	v_rcp_f32_e32 v89, v74
	v_mul_f32_e32 v74, 0xbfb8aa3b, v70
	v_exp_f32_e32 v74, v74
	v_pk_mul_f32 v[64:65], v[64:65], v[88:89]
	v_add_f32_e32 v74, 1.0, v74
	v_rcp_f32_e32 v90, v74
	v_mul_f32_e32 v74, 0xbfb8aa3b, v66
	v_exp_f32_e32 v74, v74
	s_nop 0
	v_add_f32_e32 v74, 1.0, v74
	v_rcp_f32_e32 v92, v74
	v_mul_f32_e32 v74, 0xbfb8aa3b, v71
	v_exp_f32_e32 v74, v74
	s_nop 0
	v_add_f32_e32 v74, 1.0, v74
	v_rcp_f32_e32 v91, v74
	v_mul_f32_e32 v74, 0xbfb8aa3b, v67
	v_exp_f32_e32 v74, v74
	v_pk_mul_f32 v[70:71], v[70:71], v[90:91]
	v_add_f32_e32 v74, 1.0, v74
	v_rcp_f32_e32 v93, v74
	s_nop 0
	v_pk_mul_f32 v[66:67], v[66:67], v[92:93]
	s_addk_i32 s8, 0x80
	s_lshr_b32 s0, s8, 4
	s_and_b32 s2, s0, 0xfc
	v_cvt_pk_bf16_f32 v67, v66, v67
	v_cvt_pk_bf16_f32 v66, v64, v65
	v_cvt_pk_bf16_f32 v64, v68, v69
	v_cvt_pk_bf16_f32 v65, v70, v71
	s_and_saveexec_b64 s[0:1], s[42:43]
	v_mul_u32_u24_e32 v68, s2, v159
	v_lshl_or_b32 v68, v192, v180, v68
	v_add_u32_e32 v212, v68, v181
	v_lshl_add_u64 v[68:69], v[212:213], 1, s[52:53]
	global_store_dwordx4 v[68:69], v[64:67], off nt
	s_nop 1
	s_or_b64 exec, exec, s[0:1]
	v_mul_f32_e32 v65, 0xbfb8aa3b, v52
	v_exp_f32_e32 v65, v65
	v_mul_f32_e32 v64, 0xbfb8aa3b, v56
	v_exp_f32_e32 v64, v64
	v_mul_f32_e32 v69, 0xbfb8aa3b, v54
	v_add_f32_e32 v65, 1.0, v65
	v_rcp_f32_e32 v66, v65
	v_mul_f32_e32 v65, 0xbfb8aa3b, v57
	v_exp_f32_e32 v65, v65
	v_add_f32_e32 v64, 1.0, v64
	v_exp_f32_e32 v69, v69
	v_rcp_f32_e32 v64, v64
	v_add_f32_e32 v65, 1.0, v65
	v_rcp_f32_e32 v65, v65
	v_add_f32_e32 v69, 1.0, v69
	v_mul_f32_e32 v67, 0xbfb8aa3b, v53
	v_mul_f32_e32 v68, 0xbfb8aa3b, v58
	v_rcp_f32_e32 v70, v69
	v_mul_f32_e32 v69, 0xbfb8aa3b, v59
	v_pk_mul_f32 v[56:57], v[56:57], v[64:65]
	v_mul_f32_e32 v64, 0xbfb8aa3b, v55
	v_exp_f32_e32 v67, v67
	v_exp_f32_e32 v68, v68
	v_exp_f32_e32 v69, v69
	v_exp_f32_e32 v64, v64
	v_add_f32_e32 v67, 1.0, v67
	v_add_f32_e32 v68, 1.0, v68
	v_add_f32_e32 v69, 1.0, v69
	v_add_f32_e32 v64, 1.0, v64
	v_rcp_f32_e32 v67, v67
	v_rcp_f32_e32 v68, v68
	v_rcp_f32_e32 v69, v69
	v_rcp_f32_e32 v71, v64
	v_pk_mul_f32 v[52:53], v[52:53], v[66:67]
	v_pk_mul_f32 v[58:59], v[58:59], v[68:69]
	v_pk_mul_f32 v[54:55], v[54:55], v[70:71]
	v_cvt_pk_bf16_f32 v55, v54, v55
	v_cvt_pk_bf16_f32 v54, v52, v53
	v_cvt_pk_bf16_f32 v52, v56, v57
	v_cvt_pk_bf16_f32 v53, v58, v59
	s_and_saveexec_b64 s[0:1], s[44:45]
	v_mul_u32_u24_e32 v56, s2, v158
	v_lshl_or_b32 v56, v192, v145, v56
	v_add_u32_e32 v212, v56, v172
	v_lshl_add_u64 v[56:57], v[212:213], 1, s[52:53]
	global_store_dwordx4 v[56:57], v[52:55], off nt
	s_nop 1
	s_or_b64 exec, exec, s[0:1]
	v_mul_f32_e32 v54, 0xbfb8aa3b, v48
	v_exp_f32_e32 v54, v54
	s_nop 0
	v_add_f32_e32 v54, 1.0, v54
	v_rcp_f32_e32 v66, v54
	v_mul_f32_e32 v54, 0xbfb8aa3b, v44
	v_exp_f32_e32 v54, v54
	s_nop 0
	v_add_f32_e32 v54, 1.0, v54
	v_rcp_f32_e32 v68, v54
	v_mul_f32_e32 v54, 0xbfb8aa3b, v49
	v_exp_f32_e32 v54, v54
	s_nop 0
	v_add_f32_e32 v54, 1.0, v54
	v_rcp_f32_e32 v67, v54
	v_mul_f32_e32 v54, 0xbfb8aa3b, v45
	v_exp_f32_e32 v54, v54
	v_pk_mul_f32 v[48:49], v[48:49], v[66:67]
	v_add_f32_e32 v54, 1.0, v54
	v_rcp_f32_e32 v69, v54
	v_mul_f32_e32 v54, 0xbfb8aa3b, v50
	v_exp_f32_e32 v54, v54
	v_pk_mul_f32 v[44:45], v[44:45], v[68:69]
	v_add_f32_e32 v54, 1.0, v54
	v_rcp_f32_e32 v70, v54
	v_mul_f32_e32 v54, 0xbfb8aa3b, v46
	v_exp_f32_e32 v54, v54
	s_nop 0
	v_add_f32_e32 v54, 1.0, v54
	v_rcp_f32_e32 v72, v54
	v_mul_f32_e32 v54, 0xbfb8aa3b, v51
	v_exp_f32_e32 v54, v54
	s_nop 0
	v_add_f32_e32 v54, 1.0, v54
	v_rcp_f32_e32 v71, v54
	v_mul_f32_e32 v54, 0xbfb8aa3b, v47
	v_exp_f32_e32 v54, v54
	v_pk_mul_f32 v[50:51], v[50:51], v[70:71]
	v_add_f32_e32 v54, 1.0, v54
	v_rcp_f32_e32 v73, v54
	s_nop 0
	v_pk_mul_f32 v[46:47], v[46:47], v[72:73]
	s_or_b32 s4, s2, 1
	v_cvt_pk_bf16_f32 v47, v46, v47
	v_cvt_pk_bf16_f32 v46, v44, v45
	v_cvt_pk_bf16_f32 v44, v48, v49
	v_cvt_pk_bf16_f32 v45, v50, v51
	s_and_saveexec_b64 s[0:1], s[42:43]
	v_mul_u32_u24_e32 v48, s4, v159
	v_lshlrev_b32_e32 v49, v180, v192
	v_add3_u32 v212, v48, v49, v181
	v_lshl_add_u64 v[48:49], v[212:213], 1, s[52:53]
	global_store_dwordx4 v[48:49], v[44:47], off nt
	s_nop 1
	s_or_b64 exec, exec, s[0:1]
	v_mul_f32_e32 v45, 0xbfb8aa3b, v32
	v_exp_f32_e32 v45, v45
	v_mul_f32_e32 v44, 0xbfb8aa3b, v36
	v_exp_f32_e32 v44, v44
	v_mul_f32_e32 v49, 0xbfb8aa3b, v34
	v_add_f32_e32 v45, 1.0, v45
	v_rcp_f32_e32 v46, v45
	v_mul_f32_e32 v45, 0xbfb8aa3b, v37
	v_exp_f32_e32 v45, v45
	v_add_f32_e32 v44, 1.0, v44
	v_exp_f32_e32 v49, v49
	v_rcp_f32_e32 v44, v44
	v_add_f32_e32 v45, 1.0, v45
	v_rcp_f32_e32 v45, v45
	v_add_f32_e32 v49, 1.0, v49
	v_mul_f32_e32 v47, 0xbfb8aa3b, v33
	v_mul_f32_e32 v48, 0xbfb8aa3b, v38
	v_rcp_f32_e32 v50, v49
	v_mul_f32_e32 v49, 0xbfb8aa3b, v39
	v_pk_mul_f32 v[36:37], v[36:37], v[44:45]
	v_mul_f32_e32 v44, 0xbfb8aa3b, v35
	v_exp_f32_e32 v47, v47
	v_exp_f32_e32 v48, v48
	v_exp_f32_e32 v49, v49
	v_exp_f32_e32 v44, v44
	v_add_f32_e32 v47, 1.0, v47
	v_add_f32_e32 v48, 1.0, v48
	v_add_f32_e32 v49, 1.0, v49
	v_add_f32_e32 v44, 1.0, v44
	v_rcp_f32_e32 v47, v47
	v_rcp_f32_e32 v48, v48
	v_rcp_f32_e32 v49, v49
	v_rcp_f32_e32 v51, v44
	v_pk_mul_f32 v[32:33], v[32:33], v[46:47]
	v_pk_mul_f32 v[38:39], v[38:39], v[48:49]
	v_pk_mul_f32 v[34:35], v[34:35], v[50:51]
	v_cvt_pk_bf16_f32 v35, v34, v35
	v_cvt_pk_bf16_f32 v34, v32, v33
	v_cvt_pk_bf16_f32 v32, v36, v37
	v_cvt_pk_bf16_f32 v33, v38, v39
	s_and_saveexec_b64 s[0:1], s[44:45]
	v_mul_u32_u24_e32 v36, s4, v158
	v_lshlrev_b32_e32 v37, v145, v192
	v_add3_u32 v212, v36, v37, v172
	v_lshl_add_u64 v[36:37], v[212:213], 1, s[52:53]
	global_store_dwordx4 v[36:37], v[32:35], off nt
	s_nop 1
	s_or_b64 exec, exec, s[0:1]
	v_mul_f32_e32 v34, 0xbfb8aa3b, v28
	v_exp_f32_e32 v34, v34
	s_nop 0
	v_add_f32_e32 v34, 1.0, v34
	v_rcp_f32_e32 v46, v34
	v_mul_f32_e32 v34, 0xbfb8aa3b, v24
	v_exp_f32_e32 v34, v34
	s_nop 0
	v_add_f32_e32 v34, 1.0, v34
	v_rcp_f32_e32 v48, v34
	v_mul_f32_e32 v34, 0xbfb8aa3b, v29
	v_exp_f32_e32 v34, v34
	s_nop 0
	v_add_f32_e32 v34, 1.0, v34
	v_rcp_f32_e32 v47, v34
	v_mul_f32_e32 v34, 0xbfb8aa3b, v25
	v_exp_f32_e32 v34, v34
	v_pk_mul_f32 v[28:29], v[28:29], v[46:47]
	v_add_f32_e32 v34, 1.0, v34
	v_rcp_f32_e32 v49, v34
	v_mul_f32_e32 v34, 0xbfb8aa3b, v30
	v_exp_f32_e32 v34, v34
	v_pk_mul_f32 v[24:25], v[24:25], v[48:49]
	v_add_f32_e32 v34, 1.0, v34
	v_rcp_f32_e32 v50, v34
	v_mul_f32_e32 v34, 0xbfb8aa3b, v26
	v_exp_f32_e32 v34, v34
	s_nop 0
	v_add_f32_e32 v34, 1.0, v34
	v_rcp_f32_e32 v52, v34
	v_mul_f32_e32 v34, 0xbfb8aa3b, v31
	v_exp_f32_e32 v34, v34
	s_nop 0
	v_add_f32_e32 v34, 1.0, v34
	v_rcp_f32_e32 v51, v34
	v_mul_f32_e32 v34, 0xbfb8aa3b, v27
	v_exp_f32_e32 v34, v34
	v_pk_mul_f32 v[30:31], v[30:31], v[50:51]
	v_add_f32_e32 v34, 1.0, v34
	v_rcp_f32_e32 v53, v34
	s_nop 0
	v_pk_mul_f32 v[26:27], v[26:27], v[52:53]
	s_or_b32 s4, s2, 2
	v_cvt_pk_bf16_f32 v27, v26, v27
	v_cvt_pk_bf16_f32 v26, v24, v25
	v_cvt_pk_bf16_f32 v24, v28, v29
	v_cvt_pk_bf16_f32 v25, v30, v31
	s_and_saveexec_b64 s[0:1], s[42:43]
	v_mul_u32_u24_e32 v28, s4, v159
	v_lshl_or_b32 v28, v192, v180, v28
	v_add_u32_e32 v212, v28, v181
	v_lshl_add_u64 v[28:29], v[212:213], 1, s[52:53]
	global_store_dwordx4 v[28:29], v[24:27], off nt
	s_nop 1
	s_or_b64 exec, exec, s[0:1]
	v_mul_f32_e32 v25, 0xbfb8aa3b, v16
	v_exp_f32_e32 v25, v25
	v_mul_f32_e32 v24, 0xbfb8aa3b, v20
	v_exp_f32_e32 v24, v24
	v_mul_f32_e32 v29, 0xbfb8aa3b, v18
	v_add_f32_e32 v25, 1.0, v25
	v_rcp_f32_e32 v26, v25
	v_mul_f32_e32 v25, 0xbfb8aa3b, v21
	v_exp_f32_e32 v25, v25
	v_add_f32_e32 v24, 1.0, v24
	v_exp_f32_e32 v29, v29
	v_rcp_f32_e32 v24, v24
	v_add_f32_e32 v25, 1.0, v25
	v_rcp_f32_e32 v25, v25
	v_add_f32_e32 v29, 1.0, v29
	v_mul_f32_e32 v27, 0xbfb8aa3b, v17
	v_mul_f32_e32 v28, 0xbfb8aa3b, v22
	v_rcp_f32_e32 v30, v29
	v_mul_f32_e32 v29, 0xbfb8aa3b, v23
	v_pk_mul_f32 v[20:21], v[20:21], v[24:25]
	v_mul_f32_e32 v24, 0xbfb8aa3b, v19
	v_exp_f32_e32 v27, v27
	v_exp_f32_e32 v28, v28
	v_exp_f32_e32 v29, v29
	v_exp_f32_e32 v24, v24
	v_add_f32_e32 v27, 1.0, v27
	v_add_f32_e32 v28, 1.0, v28
	v_add_f32_e32 v29, 1.0, v29
	v_add_f32_e32 v24, 1.0, v24
	v_rcp_f32_e32 v27, v27
	v_rcp_f32_e32 v28, v28
	v_rcp_f32_e32 v29, v29
	v_rcp_f32_e32 v31, v24
	v_pk_mul_f32 v[16:17], v[16:17], v[26:27]
	v_pk_mul_f32 v[22:23], v[22:23], v[28:29]
	v_pk_mul_f32 v[18:19], v[18:19], v[30:31]
	v_cvt_pk_bf16_f32 v19, v18, v19
	v_cvt_pk_bf16_f32 v18, v16, v17
	v_cvt_pk_bf16_f32 v16, v20, v21
	v_cvt_pk_bf16_f32 v17, v22, v23
	s_and_saveexec_b64 s[0:1], s[44:45]
	v_mul_u32_u24_e32 v20, s4, v158
	v_lshl_or_b32 v20, v192, v145, v20
	v_add_u32_e32 v212, v20, v172
	v_lshl_add_u64 v[20:21], v[212:213], 1, s[52:53]
	global_store_dwordx4 v[20:21], v[16:19], off nt
	s_nop 1
	s_or_b64 exec, exec, s[0:1]
	v_mul_f32_e32 v18, 0xbfb8aa3b, v12
	v_exp_f32_e32 v18, v18
	s_nop 0
	v_add_f32_e32 v18, 1.0, v18
	v_rcp_f32_e32 v26, v18
	v_mul_f32_e32 v18, 0xbfb8aa3b, v8
	v_exp_f32_e32 v18, v18
	s_nop 0
	v_add_f32_e32 v18, 1.0, v18
	v_rcp_f32_e32 v28, v18
	v_mul_f32_e32 v18, 0xbfb8aa3b, v13
	v_exp_f32_e32 v18, v18
	s_nop 0
	v_add_f32_e32 v18, 1.0, v18
	v_rcp_f32_e32 v27, v18
	v_mul_f32_e32 v18, 0xbfb8aa3b, v9
	v_exp_f32_e32 v18, v18
	v_pk_mul_f32 v[12:13], v[12:13], v[26:27]
	v_add_f32_e32 v18, 1.0, v18
	v_rcp_f32_e32 v29, v18
	v_mul_f32_e32 v18, 0xbfb8aa3b, v14
	v_exp_f32_e32 v18, v18
	v_pk_mul_f32 v[8:9], v[8:9], v[28:29]
	v_add_f32_e32 v18, 1.0, v18
	v_rcp_f32_e32 v30, v18
	v_mul_f32_e32 v18, 0xbfb8aa3b, v10
	v_exp_f32_e32 v18, v18
	s_nop 0
	v_add_f32_e32 v18, 1.0, v18
	v_rcp_f32_e32 v32, v18
	v_mul_f32_e32 v18, 0xbfb8aa3b, v15
	v_exp_f32_e32 v18, v18
	s_nop 0
	v_add_f32_e32 v18, 1.0, v18
	v_rcp_f32_e32 v31, v18
	v_mul_f32_e32 v18, 0xbfb8aa3b, v11
	v_exp_f32_e32 v18, v18
	v_pk_mul_f32 v[14:15], v[14:15], v[30:31]
	v_add_f32_e32 v18, 1.0, v18
	v_rcp_f32_e32 v33, v18
	s_nop 0
	v_pk_mul_f32 v[10:11], v[10:11], v[32:33]
	s_or_b32 s2, s2, 3
	v_cvt_pk_bf16_f32 v11, v10, v11
	v_cvt_pk_bf16_f32 v10, v8, v9
	v_cvt_pk_bf16_f32 v8, v12, v13
	v_cvt_pk_bf16_f32 v9, v14, v15
	s_and_saveexec_b64 s[0:1], s[42:43]
	v_mul_u32_u24_e32 v12, s2, v159
	v_lshlrev_b32_e32 v13, v180, v192
	v_add3_u32 v212, v12, v13, v181
	v_lshl_add_u64 v[12:13], v[212:213], 1, s[52:53]
	global_store_dwordx4 v[12:13], v[8:11], off nt
	s_nop 1
	s_or_b64 exec, exec, s[0:1]
	s_and_b64 vcc, exec, s[38:39]
	v_mul_f32_e32 v9, 0xbfb8aa3b, v0
	v_exp_f32_e32 v9, v9
	v_mul_f32_e32 v8, 0xbfb8aa3b, v4
	v_exp_f32_e32 v8, v8
	v_mul_f32_e32 v13, 0xbfb8aa3b, v2
	v_add_f32_e32 v9, 1.0, v9
	v_rcp_f32_e32 v10, v9
	v_mul_f32_e32 v9, 0xbfb8aa3b, v5
	v_exp_f32_e32 v9, v9
	v_add_f32_e32 v8, 1.0, v8
	v_exp_f32_e32 v13, v13
	v_rcp_f32_e32 v8, v8
	v_add_f32_e32 v9, 1.0, v9
	v_rcp_f32_e32 v9, v9
	v_add_f32_e32 v13, 1.0, v13
	v_mul_f32_e32 v11, 0xbfb8aa3b, v1
	v_mul_f32_e32 v12, 0xbfb8aa3b, v6
	v_rcp_f32_e32 v14, v13
	v_mul_f32_e32 v13, 0xbfb8aa3b, v7
	v_pk_mul_f32 v[4:5], v[4:5], v[8:9]
	v_mul_f32_e32 v8, 0xbfb8aa3b, v3
	v_exp_f32_e32 v11, v11
	v_exp_f32_e32 v12, v12
	v_exp_f32_e32 v13, v13
	v_exp_f32_e32 v8, v8
	v_add_f32_e32 v11, 1.0, v11
	v_add_f32_e32 v12, 1.0, v12
	v_add_f32_e32 v13, 1.0, v13
	v_add_f32_e32 v8, 1.0, v8
	v_rcp_f32_e32 v11, v11
	v_rcp_f32_e32 v12, v12
	v_rcp_f32_e32 v13, v13
	v_rcp_f32_e32 v15, v8
	v_pk_mul_f32 v[0:1], v[0:1], v[10:11]
	v_pk_mul_f32 v[6:7], v[6:7], v[12:13]
	v_pk_mul_f32 v[2:3], v[2:3], v[14:15]
	v_cvt_pk_bf16_f32 v3, v2, v3
	v_cvt_pk_bf16_f32 v2, v0, v1
	v_cvt_pk_bf16_f32 v0, v4, v5
	v_cvt_pk_bf16_f32 v1, v6, v7
	s_and_saveexec_b64 s[0:1], s[44:45]
	v_mul_u32_u24_e32 v4, s2, v158
	v_lshlrev_b32_e32 v5, v145, v192
	v_add3_u32 v212, v4, v5, v172
	v_lshl_add_u64 v[4:5], v[212:213], 1, s[52:53]
	global_store_dwordx4 v[4:5], v[0:3], off nt
	s_nop 1
